# v17 + attention unit epilogue rewritten by hand: per-row RMSNorm reductions of the 16 rows batched instead of 80 serial ds_bpermute round trips
# speedup vs baseline: 1.0205x; 1.0068x over previous
.LBB0_638:
	s_or_b64 exec, exec, s[4:5]
	s_lshl_b64 s[4:5], s[16:17], 12
	s_add_u32 s4, s88, s4
	s_addc_u32 s5, s89, s5
	s_lshl_b32 s16, s65, 1
	s_add_u32 s4, s4, s16
	s_addc_u32 s5, s5, 0
	s_add_u32 s4, s4, s14
	s_addc_u32 s5, s5, s15
	v_lshl_add_u32 v209, v177, 4, s23
	v_lshlrev_b32_e32 v248, 2, v176
	global_load_dword v250, v248, s[42:43]
	global_load_dword v251, v248, s[42:43] offset:128
	global_load_dword v154, v248, s[42:43] offset:256
	global_load_dword v155, v248, s[42:43] offset:384
	s_waitcnt lgkmcnt(0)
	ds_read2_b32 v[210:211], v209 offset0:0 offset1:32
	ds_read2_b32 v[212:213], v209 offset0:1 offset1:33
	ds_read2_b32 v[214:215], v209 offset0:2 offset1:34
	ds_read2_b32 v[216:217], v209 offset0:3 offset1:35
	ds_read2_b32 v[218:219], v209 offset0:8 offset1:40
	ds_read2_b32 v[220:221], v209 offset0:9 offset1:41
	ds_read2_b32 v[222:223], v209 offset0:10 offset1:42
	ds_read2_b32 v[224:225], v209 offset0:11 offset1:43
	s_waitcnt lgkmcnt(0)
	ds_read2_b32 v[226:227], v209 offset0:16 offset1:48
	ds_read2_b32 v[228:229], v209 offset0:17 offset1:49
	ds_read2_b32 v[230:231], v209 offset0:18 offset1:50
	ds_read2_b32 v[232:233], v209 offset0:19 offset1:51
	ds_read2_b32 v[234:235], v209 offset0:24 offset1:56
	ds_read2_b32 v[236:237], v209 offset0:25 offset1:57
	ds_read2_b32 v[238:239], v209 offset0:26 offset1:58
	ds_read2_b32 v[240:241], v209 offset0:27 offset1:59
	v_xor_b32_e32 v242, 1, v202
	v_lshlrev_b32_e32 v242, 2, v242
	v_xor_b32_e32 v243, 2, v202
	v_lshlrev_b32_e32 v243, 2, v243
	v_xor_b32_e32 v244, 4, v202
	v_lshlrev_b32_e32 v244, 2, v244
	v_xor_b32_e32 v245, 8, v202
	v_lshlrev_b32_e32 v245, 2, v245
	v_xor_b32_e32 v246, 16, v202
	v_lshlrev_b32_e32 v246, 2, v246
	v_lshlrev_b32_e32 v247, 1, v176
	v_lshl_add_u32 v247, v177, 14, v247
	s_waitcnt lgkmcnt(0)
	v_mul_f32_e32 v50, v50, v211
	v_mul_f32_e32 v34, v34, v211
	v_mul_f32_e32 v18, v18, v211
	v_mul_f32_e32 v2, v2, v211
	v_fma_f32 v82, v82, v210, -v50
	v_fma_f32 v66, v66, v210, -v34
	v_fma_f32 v98, v98, v210, -v18
	v_fma_f32 v114, v114, v210, -v2
	v_mul_f32_e32 v50, v82, v82
	v_mul_f32_e32 v34, v66, v66
	v_mul_f32_e32 v18, v98, v98
	v_mul_f32_e32 v2, v114, v114
	v_add_f32_e32 v130, v50, v34
	v_add_f32_e32 v130, v18, v130
	v_add_f32_e32 v130, v2, v130
	v_mul_f32_e32 v51, v51, v213
	v_mul_f32_e32 v35, v35, v213
	v_mul_f32_e32 v19, v19, v213
	v_mul_f32_e32 v3, v3, v213
	v_fma_f32 v83, v83, v212, -v51
	v_fma_f32 v67, v67, v212, -v35
	v_fma_f32 v99, v99, v212, -v19
	v_fma_f32 v115, v115, v212, -v3
	v_mul_f32_e32 v51, v83, v83
	v_mul_f32_e32 v35, v67, v67
	v_mul_f32_e32 v19, v99, v99
	v_mul_f32_e32 v3, v115, v115
	v_add_f32_e32 v131, v51, v35
	v_add_f32_e32 v131, v19, v131
	v_add_f32_e32 v131, v3, v131
	v_mul_f32_e32 v52, v52, v215
	v_mul_f32_e32 v36, v36, v215
	v_mul_f32_e32 v20, v20, v215
	v_mul_f32_e32 v4, v4, v215
	v_fma_f32 v84, v84, v214, -v52
	v_fma_f32 v68, v68, v214, -v36
	v_fma_f32 v100, v100, v214, -v20
	v_fma_f32 v116, v116, v214, -v4
	v_mul_f32_e32 v52, v84, v84
	v_mul_f32_e32 v36, v68, v68
	v_mul_f32_e32 v20, v100, v100
	v_mul_f32_e32 v4, v116, v116
	v_add_f32_e32 v132, v52, v36
	v_add_f32_e32 v132, v20, v132
	v_add_f32_e32 v132, v4, v132
	v_mul_f32_e32 v53, v53, v217
	v_mul_f32_e32 v37, v37, v217
	v_mul_f32_e32 v21, v21, v217
	v_mul_f32_e32 v5, v5, v217
	v_fma_f32 v85, v85, v216, -v53
	v_fma_f32 v69, v69, v216, -v37
	v_fma_f32 v101, v101, v216, -v21
	v_fma_f32 v117, v117, v216, -v5
	v_mul_f32_e32 v53, v85, v85
	v_mul_f32_e32 v37, v69, v69
	v_mul_f32_e32 v21, v101, v101
	v_mul_f32_e32 v5, v117, v117
	v_add_f32_e32 v133, v53, v37
	v_add_f32_e32 v133, v21, v133
	v_add_f32_e32 v133, v5, v133
	v_mul_f32_e32 v54, v54, v219
	v_mul_f32_e32 v38, v38, v219
	v_mul_f32_e32 v22, v22, v219
	v_mul_f32_e32 v6, v6, v219
	v_fma_f32 v86, v86, v218, -v54
	v_fma_f32 v70, v70, v218, -v38
	v_fma_f32 v102, v102, v218, -v22
	v_fma_f32 v118, v118, v218, -v6
	v_mul_f32_e32 v54, v86, v86
	v_mul_f32_e32 v38, v70, v70
	v_mul_f32_e32 v22, v102, v102
	v_mul_f32_e32 v6, v118, v118
	v_add_f32_e32 v134, v54, v38
	v_add_f32_e32 v134, v22, v134
	v_add_f32_e32 v134, v6, v134
	v_mul_f32_e32 v55, v55, v221
	v_mul_f32_e32 v39, v39, v221
	v_mul_f32_e32 v23, v23, v221
	v_mul_f32_e32 v7, v7, v221
	v_fma_f32 v87, v87, v220, -v55
	v_fma_f32 v71, v71, v220, -v39
	v_fma_f32 v103, v103, v220, -v23
	v_fma_f32 v119, v119, v220, -v7
	v_mul_f32_e32 v55, v87, v87
	v_mul_f32_e32 v39, v71, v71
	v_mul_f32_e32 v23, v103, v103
	v_mul_f32_e32 v7, v119, v119
	v_add_f32_e32 v135, v55, v39
	v_add_f32_e32 v135, v23, v135
	v_add_f32_e32 v135, v7, v135
	v_mul_f32_e32 v56, v56, v223
	v_mul_f32_e32 v40, v40, v223
	v_mul_f32_e32 v24, v24, v223
	v_mul_f32_e32 v8, v8, v223
	v_fma_f32 v88, v88, v222, -v56
	v_fma_f32 v72, v72, v222, -v40
	v_fma_f32 v104, v104, v222, -v24
	v_fma_f32 v120, v120, v222, -v8
	v_mul_f32_e32 v56, v88, v88
	v_mul_f32_e32 v40, v72, v72
	v_mul_f32_e32 v24, v104, v104
	v_mul_f32_e32 v8, v120, v120
	v_add_f32_e32 v136, v56, v40
	v_add_f32_e32 v136, v24, v136
	v_add_f32_e32 v136, v8, v136
	v_mul_f32_e32 v57, v57, v225
	v_mul_f32_e32 v41, v41, v225
	v_mul_f32_e32 v25, v25, v225
	v_mul_f32_e32 v9, v9, v225
	v_fma_f32 v89, v89, v224, -v57
	v_fma_f32 v73, v73, v224, -v41
	v_fma_f32 v105, v105, v224, -v25
	v_fma_f32 v121, v121, v224, -v9
	v_mul_f32_e32 v57, v89, v89
	v_mul_f32_e32 v41, v73, v73
	v_mul_f32_e32 v25, v105, v105
	v_mul_f32_e32 v9, v121, v121
	v_add_f32_e32 v137, v57, v41
	v_add_f32_e32 v137, v25, v137
	v_add_f32_e32 v137, v9, v137
	v_mul_f32_e32 v58, v58, v227
	v_mul_f32_e32 v42, v42, v227
	v_mul_f32_e32 v26, v26, v227
	v_mul_f32_e32 v10, v10, v227
	v_fma_f32 v90, v90, v226, -v58
	v_fma_f32 v74, v74, v226, -v42
	v_fma_f32 v106, v106, v226, -v26
	v_fma_f32 v122, v122, v226, -v10
	v_mul_f32_e32 v58, v90, v90
	v_mul_f32_e32 v42, v74, v74
	v_mul_f32_e32 v26, v106, v106
	v_mul_f32_e32 v10, v122, v122
	v_add_f32_e32 v138, v58, v42
	v_add_f32_e32 v138, v26, v138
	v_add_f32_e32 v138, v10, v138
	v_mul_f32_e32 v59, v59, v229
	v_mul_f32_e32 v43, v43, v229
	v_mul_f32_e32 v27, v27, v229
	v_mul_f32_e32 v11, v11, v229
	v_fma_f32 v91, v91, v228, -v59
	v_fma_f32 v75, v75, v228, -v43
	v_fma_f32 v107, v107, v228, -v27
	v_fma_f32 v123, v123, v228, -v11
	v_mul_f32_e32 v59, v91, v91
	v_mul_f32_e32 v43, v75, v75
	v_mul_f32_e32 v27, v107, v107
	v_mul_f32_e32 v11, v123, v123
	v_add_f32_e32 v139, v59, v43
	v_add_f32_e32 v139, v27, v139
	v_add_f32_e32 v139, v11, v139
	v_mul_f32_e32 v60, v60, v231
	v_mul_f32_e32 v44, v44, v231
	v_mul_f32_e32 v28, v28, v231
	v_mul_f32_e32 v12, v12, v231
	v_fma_f32 v92, v92, v230, -v60
	v_fma_f32 v76, v76, v230, -v44
	v_fma_f32 v108, v108, v230, -v28
	v_fma_f32 v124, v124, v230, -v12
	v_mul_f32_e32 v60, v92, v92
	v_mul_f32_e32 v44, v76, v76
	v_mul_f32_e32 v28, v108, v108
	v_mul_f32_e32 v12, v124, v124
	v_add_f32_e32 v140, v60, v44
	v_add_f32_e32 v140, v28, v140
	v_add_f32_e32 v140, v12, v140
	v_mul_f32_e32 v61, v61, v233
	v_mul_f32_e32 v45, v45, v233
	v_mul_f32_e32 v29, v29, v233
	v_mul_f32_e32 v13, v13, v233
	v_fma_f32 v93, v93, v232, -v61
	v_fma_f32 v77, v77, v232, -v45
	v_fma_f32 v109, v109, v232, -v29
	v_fma_f32 v125, v125, v232, -v13
	v_mul_f32_e32 v61, v93, v93
	v_mul_f32_e32 v45, v77, v77
	v_mul_f32_e32 v29, v109, v109
	v_mul_f32_e32 v13, v125, v125
	v_add_f32_e32 v141, v61, v45
	v_add_f32_e32 v141, v29, v141
	v_add_f32_e32 v141, v13, v141
	v_mul_f32_e32 v62, v62, v235
	v_mul_f32_e32 v46, v46, v235
	v_mul_f32_e32 v30, v30, v235
	v_mul_f32_e32 v14, v14, v235
	v_fma_f32 v94, v94, v234, -v62
	v_fma_f32 v78, v78, v234, -v46
	v_fma_f32 v110, v110, v234, -v30
	v_fma_f32 v126, v126, v234, -v14
	v_mul_f32_e32 v62, v94, v94
	v_mul_f32_e32 v46, v78, v78
	v_mul_f32_e32 v30, v110, v110
	v_mul_f32_e32 v14, v126, v126
	v_add_f32_e32 v142, v62, v46
	v_add_f32_e32 v142, v30, v142
	v_add_f32_e32 v142, v14, v142
	v_mul_f32_e32 v63, v63, v237
	v_mul_f32_e32 v47, v47, v237
	v_mul_f32_e32 v31, v31, v237
	v_mul_f32_e32 v15, v15, v237
	v_fma_f32 v95, v95, v236, -v63
	v_fma_f32 v79, v79, v236, -v47
	v_fma_f32 v111, v111, v236, -v31
	v_fma_f32 v127, v127, v236, -v15
	v_mul_f32_e32 v63, v95, v95
	v_mul_f32_e32 v47, v79, v79
	v_mul_f32_e32 v31, v111, v111
	v_mul_f32_e32 v15, v127, v127
	v_add_f32_e32 v143, v63, v47
	v_add_f32_e32 v143, v31, v143
	v_add_f32_e32 v143, v15, v143
	v_mul_f32_e32 v64, v64, v239
	v_mul_f32_e32 v48, v48, v239
	v_mul_f32_e32 v32, v32, v239
	v_mul_f32_e32 v16, v16, v239
	v_fma_f32 v96, v96, v238, -v64
	v_fma_f32 v80, v80, v238, -v48
	v_fma_f32 v112, v112, v238, -v32
	v_fma_f32 v128, v128, v238, -v16
	v_mul_f32_e32 v64, v96, v96
	v_mul_f32_e32 v48, v80, v80
	v_mul_f32_e32 v32, v112, v112
	v_mul_f32_e32 v16, v128, v128
	v_add_f32_e32 v144, v64, v48
	v_add_f32_e32 v144, v32, v144
	v_add_f32_e32 v144, v16, v144
	v_mul_f32_e32 v65, v65, v241
	v_mul_f32_e32 v49, v49, v241
	v_mul_f32_e32 v33, v33, v241
	v_mul_f32_e32 v17, v17, v241
	v_fma_f32 v97, v97, v240, -v65
	v_fma_f32 v81, v81, v240, -v49
	v_fma_f32 v113, v113, v240, -v33
	v_fma_f32 v129, v129, v240, -v17
	v_mul_f32_e32 v65, v97, v97
	v_mul_f32_e32 v49, v81, v81
	v_mul_f32_e32 v33, v113, v113
	v_mul_f32_e32 v17, v129, v129
	v_add_f32_e32 v145, v65, v49
	v_add_f32_e32 v145, v33, v145
	v_add_f32_e32 v145, v17, v145
	ds_bpermute_b32 v146, v242, v130
	ds_bpermute_b32 v147, v242, v131
	ds_bpermute_b32 v148, v242, v132
	ds_bpermute_b32 v149, v242, v133
	ds_bpermute_b32 v150, v242, v134
	ds_bpermute_b32 v151, v242, v135
	ds_bpermute_b32 v152, v242, v136
	ds_bpermute_b32 v153, v242, v137
	s_waitcnt lgkmcnt(0)
	v_add_f32_e32 v130, v130, v146
	v_add_f32_e32 v131, v131, v147
	v_add_f32_e32 v132, v132, v148
	v_add_f32_e32 v133, v133, v149
	v_add_f32_e32 v134, v134, v150
	v_add_f32_e32 v135, v135, v151
	v_add_f32_e32 v136, v136, v152
	v_add_f32_e32 v137, v137, v153
	ds_bpermute_b32 v146, v243, v130
	ds_bpermute_b32 v147, v243, v131
	ds_bpermute_b32 v148, v243, v132
	ds_bpermute_b32 v149, v243, v133
	ds_bpermute_b32 v150, v243, v134
	ds_bpermute_b32 v151, v243, v135
	ds_bpermute_b32 v152, v243, v136
	ds_bpermute_b32 v153, v243, v137
	s_waitcnt lgkmcnt(0)
	v_add_f32_e32 v130, v130, v146
	v_add_f32_e32 v131, v131, v147
	v_add_f32_e32 v132, v132, v148
	v_add_f32_e32 v133, v133, v149
	v_add_f32_e32 v134, v134, v150
	v_add_f32_e32 v135, v135, v151
	v_add_f32_e32 v136, v136, v152
	v_add_f32_e32 v137, v137, v153
	ds_bpermute_b32 v146, v244, v130
	ds_bpermute_b32 v147, v244, v131
	ds_bpermute_b32 v148, v244, v132
	ds_bpermute_b32 v149, v244, v133
	ds_bpermute_b32 v150, v244, v134
	ds_bpermute_b32 v151, v244, v135
	ds_bpermute_b32 v152, v244, v136
	ds_bpermute_b32 v153, v244, v137
	s_waitcnt lgkmcnt(0)
	v_add_f32_e32 v130, v130, v146
	v_add_f32_e32 v131, v131, v147
	v_add_f32_e32 v132, v132, v148
	v_add_f32_e32 v133, v133, v149
	v_add_f32_e32 v134, v134, v150
	v_add_f32_e32 v135, v135, v151
	v_add_f32_e32 v136, v136, v152
	v_add_f32_e32 v137, v137, v153
	ds_bpermute_b32 v146, v245, v130
	ds_bpermute_b32 v147, v245, v131
	ds_bpermute_b32 v148, v245, v132
	ds_bpermute_b32 v149, v245, v133
	ds_bpermute_b32 v150, v245, v134
	ds_bpermute_b32 v151, v245, v135
	ds_bpermute_b32 v152, v245, v136
	ds_bpermute_b32 v153, v245, v137
	s_waitcnt lgkmcnt(0)
	v_add_f32_e32 v130, v130, v146
	v_add_f32_e32 v131, v131, v147
	v_add_f32_e32 v132, v132, v148
	v_add_f32_e32 v133, v133, v149
	v_add_f32_e32 v134, v134, v150
	v_add_f32_e32 v135, v135, v151
	v_add_f32_e32 v136, v136, v152
	v_add_f32_e32 v137, v137, v153
	ds_bpermute_b32 v146, v246, v130
	ds_bpermute_b32 v147, v246, v131
	ds_bpermute_b32 v148, v246, v132
	ds_bpermute_b32 v149, v246, v133
	ds_bpermute_b32 v150, v246, v134
	ds_bpermute_b32 v151, v246, v135
	ds_bpermute_b32 v152, v246, v136
	ds_bpermute_b32 v153, v246, v137
	s_waitcnt lgkmcnt(0)
	v_add_f32_e32 v130, v130, v146
	v_add_f32_e32 v131, v131, v147
	v_add_f32_e32 v132, v132, v148
	v_add_f32_e32 v133, v133, v149
	v_add_f32_e32 v134, v134, v150
	v_add_f32_e32 v135, v135, v151
	v_add_f32_e32 v136, v136, v152
	v_add_f32_e32 v137, v137, v153
	ds_bpermute_b32 v146, v242, v138
	ds_bpermute_b32 v147, v242, v139
	ds_bpermute_b32 v148, v242, v140
	ds_bpermute_b32 v149, v242, v141
	ds_bpermute_b32 v150, v242, v142
	ds_bpermute_b32 v151, v242, v143
	ds_bpermute_b32 v152, v242, v144
	ds_bpermute_b32 v153, v242, v145
	s_waitcnt lgkmcnt(0)
	v_add_f32_e32 v138, v138, v146
	v_add_f32_e32 v139, v139, v147
	v_add_f32_e32 v140, v140, v148
	v_add_f32_e32 v141, v141, v149
	v_add_f32_e32 v142, v142, v150
	v_add_f32_e32 v143, v143, v151
	v_add_f32_e32 v144, v144, v152
	v_add_f32_e32 v145, v145, v153
	ds_bpermute_b32 v146, v243, v138
	ds_bpermute_b32 v147, v243, v139
	ds_bpermute_b32 v148, v243, v140
	ds_bpermute_b32 v149, v243, v141
	ds_bpermute_b32 v150, v243, v142
	ds_bpermute_b32 v151, v243, v143
	ds_bpermute_b32 v152, v243, v144
	ds_bpermute_b32 v153, v243, v145
	s_waitcnt lgkmcnt(0)
	v_add_f32_e32 v138, v138, v146
	v_add_f32_e32 v139, v139, v147
	v_add_f32_e32 v140, v140, v148
	v_add_f32_e32 v141, v141, v149
	v_add_f32_e32 v142, v142, v150
	v_add_f32_e32 v143, v143, v151
	v_add_f32_e32 v144, v144, v152
	v_add_f32_e32 v145, v145, v153
	ds_bpermute_b32 v146, v244, v138
	ds_bpermute_b32 v147, v244, v139
	ds_bpermute_b32 v148, v244, v140
	ds_bpermute_b32 v149, v244, v141
	ds_bpermute_b32 v150, v244, v142
	ds_bpermute_b32 v151, v244, v143
	ds_bpermute_b32 v152, v244, v144
	ds_bpermute_b32 v153, v244, v145
	s_waitcnt lgkmcnt(0)
	v_add_f32_e32 v138, v138, v146
	v_add_f32_e32 v139, v139, v147
	v_add_f32_e32 v140, v140, v148
	v_add_f32_e32 v141, v141, v149
	v_add_f32_e32 v142, v142, v150
	v_add_f32_e32 v143, v143, v151
	v_add_f32_e32 v144, v144, v152
	v_add_f32_e32 v145, v145, v153
	ds_bpermute_b32 v146, v245, v138
	ds_bpermute_b32 v147, v245, v139
	ds_bpermute_b32 v148, v245, v140
	ds_bpermute_b32 v149, v245, v141
	ds_bpermute_b32 v150, v245, v142
	ds_bpermute_b32 v151, v245, v143
	ds_bpermute_b32 v152, v245, v144
	ds_bpermute_b32 v153, v245, v145
	s_waitcnt lgkmcnt(0)
	v_add_f32_e32 v138, v138, v146
	v_add_f32_e32 v139, v139, v147
	v_add_f32_e32 v140, v140, v148
	v_add_f32_e32 v141, v141, v149
	v_add_f32_e32 v142, v142, v150
	v_add_f32_e32 v143, v143, v151
	v_add_f32_e32 v144, v144, v152
	v_add_f32_e32 v145, v145, v153
	ds_bpermute_b32 v146, v246, v138
	ds_bpermute_b32 v147, v246, v139
	ds_bpermute_b32 v148, v246, v140
	ds_bpermute_b32 v149, v246, v141
	ds_bpermute_b32 v150, v246, v142
	ds_bpermute_b32 v151, v246, v143
	ds_bpermute_b32 v152, v246, v144
	ds_bpermute_b32 v153, v246, v145
	s_waitcnt lgkmcnt(0)
	v_add_f32_e32 v138, v138, v146
	v_add_f32_e32 v139, v139, v147
	v_add_f32_e32 v140, v140, v148
	v_add_f32_e32 v141, v141, v149
	v_add_f32_e32 v142, v142, v150
	v_add_f32_e32 v143, v143, v151
	v_add_f32_e32 v144, v144, v152
	v_add_f32_e32 v145, v145, v153
	s_waitcnt vmcnt(0)
	v_mul_f32_e32 v156, 0x3f4ccccd, v250
	v_mul_f32_e32 v157, 0x3f4ccccd, v251
	v_mul_f32_e32 v158, 0x3f4ccccd, v154
	v_mul_f32_e32 v159, 0x3f4ccccd, v155
	v_fmamk_f32 v130, v130, 0x3c000000, v203
	v_fmamk_f32 v131, v131, 0x3c000000, v203
	v_fmamk_f32 v132, v132, 0x3c000000, v203
	v_fmamk_f32 v133, v133, 0x3c000000, v203
	v_fmamk_f32 v134, v134, 0x3c000000, v203
	v_fmamk_f32 v135, v135, 0x3c000000, v203
	v_fmamk_f32 v136, v136, 0x3c000000, v203
	v_fmamk_f32 v137, v137, 0x3c000000, v203
	v_fmamk_f32 v138, v138, 0x3c000000, v203
	v_fmamk_f32 v139, v139, 0x3c000000, v203
	v_fmamk_f32 v140, v140, 0x3c000000, v203
	v_fmamk_f32 v141, v141, 0x3c000000, v203
	v_fmamk_f32 v142, v142, 0x3c000000, v203
	v_fmamk_f32 v143, v143, 0x3c000000, v203
	v_fmamk_f32 v144, v144, 0x3c000000, v203
	v_fmamk_f32 v145, v145, 0x3c000000, v203
	v_rsq_f32_e32 v130, v130
	v_rsq_f32_e32 v131, v131
	v_rsq_f32_e32 v132, v132
	v_rsq_f32_e32 v133, v133
	v_rsq_f32_e32 v134, v134
	v_rsq_f32_e32 v135, v135
	v_rsq_f32_e32 v136, v136
	v_rsq_f32_e32 v137, v137
	v_rsq_f32_e32 v138, v138
	v_rsq_f32_e32 v139, v139
	v_rsq_f32_e32 v140, v140
	v_rsq_f32_e32 v141, v141
	v_rsq_f32_e32 v142, v142
	v_rsq_f32_e32 v143, v143
	v_rsq_f32_e32 v144, v144
	v_rsq_f32_e32 v145, v145
	s_add_u32 s18, s4, 0x0
	s_addc_u32 s19, s5, 0
	v_mul_f32_e32 v82, v82, v130
	v_mul_f32_e32 v66, v66, v130
	v_mul_f32_e32 v98, v98, v130
	v_mul_f32_e32 v114, v114, v130
	v_mul_f32_e32 v82, v156, v82
	v_mul_f32_e32 v66, v157, v66
	v_mul_f32_e32 v98, v158, v98
	v_mul_f32_e32 v114, v159, v114
	v_cvt_pk_bf16_f32 v82, v82, v163
	v_cvt_pk_bf16_f32 v66, v66, v163
	v_cvt_pk_bf16_f32 v98, v98, v163
	v_cvt_pk_bf16_f32 v114, v114, v163
	global_store_short v247, v82, s[18:19]
	global_store_short v247, v66, s[18:19] offset:64
	global_store_short v247, v98, s[18:19] offset:128
	global_store_short v247, v114, s[18:19] offset:192
	s_add_u32 s18, s4, 0x1000
	s_addc_u32 s19, s5, 0
	v_mul_f32_e32 v83, v83, v131
	v_mul_f32_e32 v67, v67, v131
	v_mul_f32_e32 v99, v99, v131
	v_mul_f32_e32 v115, v115, v131
	v_mul_f32_e32 v83, v156, v83
	v_mul_f32_e32 v67, v157, v67
	v_mul_f32_e32 v99, v158, v99
	v_mul_f32_e32 v115, v159, v115
	v_cvt_pk_bf16_f32 v83, v83, v163
	v_cvt_pk_bf16_f32 v67, v67, v163
	v_cvt_pk_bf16_f32 v99, v99, v163
	v_cvt_pk_bf16_f32 v115, v115, v163
	global_store_short v247, v83, s[18:19]
	global_store_short v247, v67, s[18:19] offset:64
	global_store_short v247, v99, s[18:19] offset:128
	global_store_short v247, v115, s[18:19] offset:192
	s_add_u32 s18, s4, 0x2000
	s_addc_u32 s19, s5, 0
	v_mul_f32_e32 v84, v84, v132
	v_mul_f32_e32 v68, v68, v132
	v_mul_f32_e32 v100, v100, v132
	v_mul_f32_e32 v116, v116, v132
	v_mul_f32_e32 v84, v156, v84
	v_mul_f32_e32 v68, v157, v68
	v_mul_f32_e32 v100, v158, v100
	v_mul_f32_e32 v116, v159, v116
	v_cvt_pk_bf16_f32 v84, v84, v163
	v_cvt_pk_bf16_f32 v68, v68, v163
	v_cvt_pk_bf16_f32 v100, v100, v163
	v_cvt_pk_bf16_f32 v116, v116, v163
	global_store_short v247, v84, s[18:19]
	global_store_short v247, v68, s[18:19] offset:64
	global_store_short v247, v100, s[18:19] offset:128
	global_store_short v247, v116, s[18:19] offset:192
	s_add_u32 s18, s4, 0x3000
	s_addc_u32 s19, s5, 0
	v_mul_f32_e32 v85, v85, v133
	v_mul_f32_e32 v69, v69, v133
	v_mul_f32_e32 v101, v101, v133
	v_mul_f32_e32 v117, v117, v133
	v_mul_f32_e32 v85, v156, v85
	v_mul_f32_e32 v69, v157, v69
	v_mul_f32_e32 v101, v158, v101
	v_mul_f32_e32 v117, v159, v117
	v_cvt_pk_bf16_f32 v85, v85, v163
	v_cvt_pk_bf16_f32 v69, v69, v163
	v_cvt_pk_bf16_f32 v101, v101, v163
	v_cvt_pk_bf16_f32 v117, v117, v163
	global_store_short v247, v85, s[18:19]
	global_store_short v247, v69, s[18:19] offset:64
	global_store_short v247, v101, s[18:19] offset:128
	global_store_short v247, v117, s[18:19] offset:192
	s_add_u32 s18, s4, 0x8000
	s_addc_u32 s19, s5, 0
	v_mul_f32_e32 v86, v86, v134
	v_mul_f32_e32 v70, v70, v134
	v_mul_f32_e32 v102, v102, v134
	v_mul_f32_e32 v118, v118, v134
	v_mul_f32_e32 v86, v156, v86
	v_mul_f32_e32 v70, v157, v70
	v_mul_f32_e32 v102, v158, v102
	v_mul_f32_e32 v118, v159, v118
	v_cvt_pk_bf16_f32 v86, v86, v163
	v_cvt_pk_bf16_f32 v70, v70, v163
	v_cvt_pk_bf16_f32 v102, v102, v163
	v_cvt_pk_bf16_f32 v118, v118, v163
	global_store_short v247, v86, s[18:19]
	global_store_short v247, v70, s[18:19] offset:64
	global_store_short v247, v102, s[18:19] offset:128
	global_store_short v247, v118, s[18:19] offset:192
	s_add_u32 s18, s4, 0x9000
	s_addc_u32 s19, s5, 0
	v_mul_f32_e32 v87, v87, v135
	v_mul_f32_e32 v71, v71, v135
	v_mul_f32_e32 v103, v103, v135
	v_mul_f32_e32 v119, v119, v135
	v_mul_f32_e32 v87, v156, v87
	v_mul_f32_e32 v71, v157, v71
	v_mul_f32_e32 v103, v158, v103
	v_mul_f32_e32 v119, v159, v119
	v_cvt_pk_bf16_f32 v87, v87, v163
	v_cvt_pk_bf16_f32 v71, v71, v163
	v_cvt_pk_bf16_f32 v103, v103, v163
	v_cvt_pk_bf16_f32 v119, v119, v163
	global_store_short v247, v87, s[18:19]
	global_store_short v247, v71, s[18:19] offset:64
	global_store_short v247, v103, s[18:19] offset:128
	global_store_short v247, v119, s[18:19] offset:192
	s_add_u32 s18, s4, 0xa000
	s_addc_u32 s19, s5, 0
	v_mul_f32_e32 v88, v88, v136
	v_mul_f32_e32 v72, v72, v136
	v_mul_f32_e32 v104, v104, v136
	v_mul_f32_e32 v120, v120, v136
	v_mul_f32_e32 v88, v156, v88
	v_mul_f32_e32 v72, v157, v72
	v_mul_f32_e32 v104, v158, v104
	v_mul_f32_e32 v120, v159, v120
	v_cvt_pk_bf16_f32 v88, v88, v163
	v_cvt_pk_bf16_f32 v72, v72, v163
	v_cvt_pk_bf16_f32 v104, v104, v163
	v_cvt_pk_bf16_f32 v120, v120, v163
	global_store_short v247, v88, s[18:19]
	global_store_short v247, v72, s[18:19] offset:64
	global_store_short v247, v104, s[18:19] offset:128
	global_store_short v247, v120, s[18:19] offset:192
	s_add_u32 s18, s4, 0xb000
	s_addc_u32 s19, s5, 0
	v_mul_f32_e32 v89, v89, v137
	v_mul_f32_e32 v73, v73, v137
	v_mul_f32_e32 v105, v105, v137
	v_mul_f32_e32 v121, v121, v137
	v_mul_f32_e32 v89, v156, v89
	v_mul_f32_e32 v73, v157, v73
	v_mul_f32_e32 v105, v158, v105
	v_mul_f32_e32 v121, v159, v121
	v_cvt_pk_bf16_f32 v89, v89, v163
	v_cvt_pk_bf16_f32 v73, v73, v163
	v_cvt_pk_bf16_f32 v105, v105, v163
	v_cvt_pk_bf16_f32 v121, v121, v163
	global_store_short v247, v89, s[18:19]
	global_store_short v247, v73, s[18:19] offset:64
	global_store_short v247, v105, s[18:19] offset:128
	global_store_short v247, v121, s[18:19] offset:192
	s_add_u32 s18, s4, 0x10000
	s_addc_u32 s19, s5, 0
	v_mul_f32_e32 v90, v90, v138
	v_mul_f32_e32 v74, v74, v138
	v_mul_f32_e32 v106, v106, v138
	v_mul_f32_e32 v122, v122, v138
	v_mul_f32_e32 v90, v156, v90
	v_mul_f32_e32 v74, v157, v74
	v_mul_f32_e32 v106, v158, v106
	v_mul_f32_e32 v122, v159, v122
	v_cvt_pk_bf16_f32 v90, v90, v163
	v_cvt_pk_bf16_f32 v74, v74, v163
	v_cvt_pk_bf16_f32 v106, v106, v163
	v_cvt_pk_bf16_f32 v122, v122, v163
	global_store_short v247, v90, s[18:19]
	global_store_short v247, v74, s[18:19] offset:64
	global_store_short v247, v106, s[18:19] offset:128
	global_store_short v247, v122, s[18:19] offset:192
	s_add_u32 s18, s4, 0x11000
	s_addc_u32 s19, s5, 0
	v_mul_f32_e32 v91, v91, v139
	v_mul_f32_e32 v75, v75, v139
	v_mul_f32_e32 v107, v107, v139
	v_mul_f32_e32 v123, v123, v139
	v_mul_f32_e32 v91, v156, v91
	v_mul_f32_e32 v75, v157, v75
	v_mul_f32_e32 v107, v158, v107
	v_mul_f32_e32 v123, v159, v123
	v_cvt_pk_bf16_f32 v91, v91, v163
	v_cvt_pk_bf16_f32 v75, v75, v163
	v_cvt_pk_bf16_f32 v107, v107, v163
	v_cvt_pk_bf16_f32 v123, v123, v163
	global_store_short v247, v91, s[18:19]
	global_store_short v247, v75, s[18:19] offset:64
	global_store_short v247, v107, s[18:19] offset:128
	global_store_short v247, v123, s[18:19] offset:192
	s_add_u32 s18, s4, 0x12000
	s_addc_u32 s19, s5, 0
	v_mul_f32_e32 v92, v92, v140
	v_mul_f32_e32 v76, v76, v140
	v_mul_f32_e32 v108, v108, v140
	v_mul_f32_e32 v124, v124, v140
	v_mul_f32_e32 v92, v156, v92
	v_mul_f32_e32 v76, v157, v76
	v_mul_f32_e32 v108, v158, v108
	v_mul_f32_e32 v124, v159, v124
	v_cvt_pk_bf16_f32 v92, v92, v163
	v_cvt_pk_bf16_f32 v76, v76, v163
	v_cvt_pk_bf16_f32 v108, v108, v163
	v_cvt_pk_bf16_f32 v124, v124, v163
	global_store_short v247, v92, s[18:19]
	global_store_short v247, v76, s[18:19] offset:64
	global_store_short v247, v108, s[18:19] offset:128
	global_store_short v247, v124, s[18:19] offset:192
	s_add_u32 s18, s4, 0x13000
	s_addc_u32 s19, s5, 0
	v_mul_f32_e32 v93, v93, v141
	v_mul_f32_e32 v77, v77, v141
	v_mul_f32_e32 v109, v109, v141
	v_mul_f32_e32 v125, v125, v141
	v_mul_f32_e32 v93, v156, v93
	v_mul_f32_e32 v77, v157, v77
	v_mul_f32_e32 v109, v158, v109
	v_mul_f32_e32 v125, v159, v125
	v_cvt_pk_bf16_f32 v93, v93, v163
	v_cvt_pk_bf16_f32 v77, v77, v163
	v_cvt_pk_bf16_f32 v109, v109, v163
	v_cvt_pk_bf16_f32 v125, v125, v163
	global_store_short v247, v93, s[18:19]
	global_store_short v247, v77, s[18:19] offset:64
	global_store_short v247, v109, s[18:19] offset:128
	global_store_short v247, v125, s[18:19] offset:192
	s_add_u32 s18, s4, 0x18000
	s_addc_u32 s19, s5, 0
	v_mul_f32_e32 v94, v94, v142
	v_mul_f32_e32 v78, v78, v142
	v_mul_f32_e32 v110, v110, v142
	v_mul_f32_e32 v126, v126, v142
	v_mul_f32_e32 v94, v156, v94
	v_mul_f32_e32 v78, v157, v78
	v_mul_f32_e32 v110, v158, v110
	v_mul_f32_e32 v126, v159, v126
	v_cvt_pk_bf16_f32 v94, v94, v163
	v_cvt_pk_bf16_f32 v78, v78, v163
	v_cvt_pk_bf16_f32 v110, v110, v163
	v_cvt_pk_bf16_f32 v126, v126, v163
	global_store_short v247, v94, s[18:19]
	global_store_short v247, v78, s[18:19] offset:64
	global_store_short v247, v110, s[18:19] offset:128
	global_store_short v247, v126, s[18:19] offset:192
	s_add_u32 s18, s4, 0x19000
	s_addc_u32 s19, s5, 0
	v_mul_f32_e32 v95, v95, v143
	v_mul_f32_e32 v79, v79, v143
	v_mul_f32_e32 v111, v111, v143
	v_mul_f32_e32 v127, v127, v143
	v_mul_f32_e32 v95, v156, v95
	v_mul_f32_e32 v79, v157, v79
	v_mul_f32_e32 v111, v158, v111
	v_mul_f32_e32 v127, v159, v127
	v_cvt_pk_bf16_f32 v95, v95, v163
	v_cvt_pk_bf16_f32 v79, v79, v163
	v_cvt_pk_bf16_f32 v111, v111, v163
	v_cvt_pk_bf16_f32 v127, v127, v163
	global_store_short v247, v95, s[18:19]
	global_store_short v247, v79, s[18:19] offset:64
	global_store_short v247, v111, s[18:19] offset:128
	global_store_short v247, v127, s[18:19] offset:192
	s_add_u32 s18, s4, 0x1a000
	s_addc_u32 s19, s5, 0
	v_mul_f32_e32 v96, v96, v144
	v_mul_f32_e32 v80, v80, v144
	v_mul_f32_e32 v112, v112, v144
	v_mul_f32_e32 v128, v128, v144
	v_mul_f32_e32 v96, v156, v96
	v_mul_f32_e32 v80, v157, v80
	v_mul_f32_e32 v112, v158, v112
	v_mul_f32_e32 v128, v159, v128
	v_cvt_pk_bf16_f32 v96, v96, v163
	v_cvt_pk_bf16_f32 v80, v80, v163
	v_cvt_pk_bf16_f32 v112, v112, v163
	v_cvt_pk_bf16_f32 v128, v128, v163
	global_store_short v247, v96, s[18:19]
	global_store_short v247, v80, s[18:19] offset:64
	global_store_short v247, v112, s[18:19] offset:128
	global_store_short v247, v128, s[18:19] offset:192
	s_add_u32 s18, s4, 0x1b000
	s_addc_u32 s19, s5, 0
	v_mul_f32_e32 v97, v97, v145
	v_mul_f32_e32 v81, v81, v145
	v_mul_f32_e32 v113, v113, v145
	v_mul_f32_e32 v129, v129, v145
	v_mul_f32_e32 v97, v156, v97
	v_mul_f32_e32 v81, v157, v81
	v_mul_f32_e32 v113, v158, v113
	v_mul_f32_e32 v129, v159, v129
	v_cvt_pk_bf16_f32 v97, v97, v163
	v_cvt_pk_bf16_f32 v81, v81, v163
	v_cvt_pk_bf16_f32 v113, v113, v163
	v_cvt_pk_bf16_f32 v129, v129, v163
	global_store_short v247, v97, s[18:19]
	global_store_short v247, v81, s[18:19] offset:64
	global_store_short v247, v113, s[18:19] offset:128
	global_store_short v247, v129, s[18:19] offset:192
	s_add_i32 s33, s33, s92
	s_cmpk_lt_i32 s33, 0x200
	s_waitcnt vmcnt(63) expcnt(7) lgkmcnt(15)
	s_barrier
	s_cbranch_scc0 .LBB0_653
